# phase 3 load balance: workgroups 0..31 (which also run the cumulative-sum items) skip the kv/k_b row-norm loop; workgroups 32..255 cover all rows with stride 1792 waves (4 or 5 rows per wave)
# baseline (speedup 1.0000x reference)
.LBB0_553:
	s_cmp_eq_u32 s80, 0x100
	s_cbranch_scc0 .Lp3_map_orig
	s_cmp_lt_u32 s2, 32
	s_cbranch_scc1 .Lp3_skip_ab
	s_sub_u32 s99, s2, 32
	v_lshl_or_b32 v2, s99, 3, v1
	s_branch .Lp3_map_done
.Lp3_skip_ab:
	s_mov_b64 s[6:7], exec
	v_readlane_b32 s82, v255, 2
	s_branch .LBB0_556

.Lp3_map_done:
	s_movk_i32 s3, 0x2000
	v_cmp_gt_i32_e32 vcc, s3, v2
	s_and_saveexec_b64 s[6:7], vcc
	v_readlane_b32 s82, v255, 2
	s_cbranch_execz .LBB0_556
	v_mbcnt_lo_u32_b32 v0, -1, 0
	v_mbcnt_hi_u32_b32 v3, -1, v0
	v_and_b32_e32 v0, 64, v3
	v_add_u32_e32 v4, 64, v0
	v_xor_b32_e32 v0, 32, v3
	v_cmp_lt_i32_e32 vcc, v0, v4
	v_xor_b32_e32 v5, 16, v3
	s_load_dwordx2 s[4:5], s[0:1], 0x58
	s_load_dwordx2 s[10:11], s[0:1], 0x68
	v_cndmask_b32_e32 v0, v3, v0, vcc
	v_cmp_lt_i32_e32 vcc, v5, v4
	s_waitcnt vmcnt(0)
	v_lshlrev_b32_e32 v6, 4, v217
	v_mov_b32_e32 v7, 0
	v_cndmask_b32_e32 v5, v3, v5, vcc
	v_lshlrev_b32_e32 v12, 2, v5
	v_xor_b32_e32 v5, 8, v3
	v_cmp_lt_i32_e32 vcc, v5, v4
	s_waitcnt lgkmcnt(0)
	s_lshl_b32 s8, s80, 3
	s_cmp_eq_u32 s80, 0x100
	s_cselect_b32 s8, 0x700, s8
	s_ashr_i32 s9, s8, 31
	v_cndmask_b32_e32 v5, v3, v5, vcc
	v_lshlrev_b32_e32 v13, 2, v5
	v_xor_b32_e32 v5, 4, v3
	v_cmp_lt_i32_e32 vcc, v5, v4
	v_lshlrev_b32_e32 v0, 2, v0
	s_lshl_b64 s[12:13], s[8:9], 9
	v_cndmask_b32_e32 v5, v3, v5, vcc
	v_lshlrev_b32_e32 v14, 2, v5
	v_xor_b32_e32 v5, 2, v3
	v_cmp_lt_i32_e32 vcc, v5, v4
	s_mov_b64 s[14:15], 0
	s_mov_b32 s3, 0x800000
	v_cndmask_b32_e32 v5, v3, v5, vcc
	v_lshlrev_b32_e32 v15, 2, v5
	v_xor_b32_e32 v5, 1, v3
	v_cmp_lt_i32_e32 vcc, v5, v4
	s_mov_b64 s[16:17], 0x21b38000
	s_mov_b32 s18, 0x21b38000
	v_cndmask_b32_e32 v3, v3, v5, vcc
	v_lshlrev_b32_e32 v16, 2, v3
	v_lshlrev_b32_e32 v3, 6, v250
	v_lshl_add_u64 v[4:5], s[4:5], 0, v[6:7]
	v_and_b32_e32 v6, 0x1c0, v3
	v_ashrrev_i32_e32 v3, 31, v2
	v_lshlrev_b64 v[8:9], 11, v[2:3]
	v_lshlrev_b64 v[10:11], 9, v[2:3]
	v_lshl_add_u64 v[6:7], s[10:11], 0, v[6:7]
	v_lshl_or_b32 v8, v217, 5, v8
	s_lshl_b64 s[10:11], s[8:9], 11
	v_lshl_or_b32 v10, v217, 3, v10
	v_mov_b32_e32 v3, 0x358637bd
	s_mov_b32 s9, 0x1ef38000
	s_movk_i32 s19, 0x1fff
	s_cmp_eq_u32 s80, 0x100
	s_cbranch_scc0 .LBB0_555
	v_readfirstlane_b32 s99, v2
	s_cmp_lt_u32 s99, 0x400
	s_cbranch_scc0 .Lp3_fast
	v_lshl_add_u64 v[22:23], s[76:77], 0, v[10:11]
	v_add_co_u32_e32 v26, vcc, 0x1e738000, v22
	global_load_dwordx4 v[18:21], v[4:5], off
	s_nop 0
	v_addc_co_u32_e32 v27, vcc, 0, v23, vcc
	global_load_dwordx2 v[26:27], v[26:27], off
	v_add_co_u32_e64 v22, s[4:5], s9, v22
	v_lshl_add_u64 v[24:25], s[76:77], 0, v[8:9]
	s_nop 0
	v_addc_co_u32_e64 v23, vcc, 0, v23, s[4:5]
	v_add_co_u32_e32 v44, vcc, s18, v24
	v_lshl_add_u64 v[42:43], v[24:25], 0, s[16:17]
	s_nop 0
	v_addc_co_u32_e32 v45, vcc, 0, v25, vcc
	v_add_u32_e32 v2, s8, v2
	v_cmp_lt_i32_e32 vcc, s19, v2
	s_or_b64 s[14:15], vcc, s[14:15]
	v_lshl_add_u64 v[8:9], v[8:9], 0, s[10:11]
	v_lshl_add_u64 v[10:11], v[10:11], 0, s[12:13]
	global_load_dwordx4 v[60:63], v[44:45], off
	global_load_dwordx4 v[64:67], v[42:43], off offset:16
	global_load_dwordx4 v[68:71], v[6:7], off
	global_load_dwordx4 v[72:75], v[6:7], off offset:16
	global_load_dwordx4 v[76:79], v[6:7], off offset:32
	global_load_dwordx4 v[80:83], v[6:7], off offset:48
	s_waitcnt vmcnt(6)
	v_lshlrev_b32_e32 v24, 16, v26
	v_and_b32_e32 v25, 0xffff0000, v26
	v_and_b32_e32 v26, 0xffff0000, v27
	v_lshlrev_b32_e32 v27, 16, v27
	v_pk_mul_f32 v[28:29], v[24:25], v[24:25]
	v_pk_mul_f32 v[30:31], v[26:27], v[26:27]
	v_add_f32_e32 v17, v28, v29
	v_add_f32_e32 v17, v31, v17
	v_add_f32_e32 v17, v30, v17
	ds_bpermute_b32 v28, v0, v17
	s_waitcnt lgkmcnt(0)
	v_add_f32_e32 v17, v17, v28
	ds_bpermute_b32 v28, v12, v17
	s_waitcnt lgkmcnt(0)
	v_add_f32_e32 v17, v17, v28
	ds_bpermute_b32 v28, v13, v17
	s_waitcnt lgkmcnt(0)
	v_add_f32_e32 v17, v17, v28
	ds_bpermute_b32 v28, v14, v17
	s_waitcnt lgkmcnt(0)
	v_add_f32_e32 v17, v17, v28
	ds_bpermute_b32 v28, v15, v17
	s_waitcnt lgkmcnt(0)
	v_add_f32_e32 v17, v17, v28
	ds_bpermute_b32 v28, v16, v17
	s_waitcnt lgkmcnt(0)
	v_add_f32_e32 v17, v17, v28
	v_fmamk_f32 v17, v17, 0x3b800000, v3
	v_mul_f32_e32 v28, 0x4b800000, v17
	v_cmp_gt_f32_e32 vcc, s3, v17
	s_nop 1
	v_cndmask_b32_e32 v17, v17, v28, vcc
	v_rsq_f32_e32 v17, v17
	s_nop 0
	v_mul_f32_e32 v28, 0x45800000, v17
	v_cndmask_b32_e32 v17, v17, v28, vcc
	v_mul_f32_e32 v24, v17, v24
	v_mul_f32_e32 v25, v17, v25
	v_mul_f32_e32 v27, v17, v27
	v_mul_f32_e32 v17, v17, v26
	v_mul_f32_e32 v18, v18, v24
	v_mul_f32_e32 v19, v19, v25
	v_mul_f32_e32 v20, v20, v27
	v_mul_f32_e32 v17, v21, v17
	v_cvt_pk_bf16_f32 v18, v18, v19
	v_cvt_pk_bf16_f32 v19, v20, v17
	global_store_dwordx2 v[22:23], v[18:19], off
	s_waitcnt vmcnt(6)
	v_and_b32_e32 v52, 0xffff0000, v60
	v_lshlrev_b32_e32 v17, 16, v60
	v_mul_f32_e32 v59, v52, v52
	v_lshlrev_b32_e32 v53, 16, v61
	v_fmac_f32_e32 v59, v17, v17
	v_and_b32_e32 v54, 0xffff0000, v61
	v_fmac_f32_e32 v59, v53, v53
	v_lshlrev_b32_e32 v55, 16, v62
	v_fmac_f32_e32 v59, v54, v54
	v_and_b32_e32 v56, 0xffff0000, v62
	v_fmac_f32_e32 v59, v55, v55
	v_lshlrev_b32_e32 v57, 16, v63
	v_fmac_f32_e32 v59, v56, v56
	v_and_b32_e32 v58, 0xffff0000, v63
	s_waitcnt vmcnt(5)
	v_and_b32_e32 v60, 0xffff0000, v64
	v_lshlrev_b32_e32 v61, 16, v64
	v_fmac_f32_e32 v59, v57, v57
	v_pk_mul_f32 v[42:43], v[60:61], v[60:61]
	v_fmac_f32_e32 v59, v58, v58
	v_and_b32_e32 v62, 0xffff0000, v65
	v_lshlrev_b32_e32 v63, 16, v65
	v_add_f32_e32 v43, v43, v59
	v_pk_mul_f32 v[46:47], v[62:63], v[62:63]
	v_add_f32_e32 v42, v42, v43
	v_and_b32_e32 v64, 0xffff0000, v66
	v_lshlrev_b32_e32 v65, 16, v66
	v_add_f32_e32 v42, v47, v42
	v_pk_mul_f32 v[48:49], v[64:65], v[64:65]
	v_add_f32_e32 v42, v46, v42
	v_and_b32_e32 v66, 0xffff0000, v67
	v_lshlrev_b32_e32 v67, 16, v67
	v_add_f32_e32 v42, v49, v42
	v_pk_mul_f32 v[50:51], v[66:67], v[66:67]
	v_add_f32_e32 v42, v48, v42
	v_add_f32_e32 v42, v51, v42
	v_add_f32_e32 v42, v50, v42
	ds_bpermute_b32 v43, v16, v42
	s_waitcnt lgkmcnt(0)
	v_add_f32_e32 v42, v42, v43
	ds_bpermute_b32 v43, v15, v42
	s_waitcnt lgkmcnt(0)
	v_add_f32_e32 v42, v42, v43
	ds_bpermute_b32 v43, v14, v42
	s_waitcnt lgkmcnt(0)
	v_add_f32_e32 v42, v42, v43
	v_fmamk_f32 v42, v42, 0x3c000000, v3
	v_mul_f32_e32 v43, 0x4b800000, v42
	v_cmp_gt_f32_e32 vcc, s3, v42
	s_nop 1
	v_cndmask_b32_e32 v42, v42, v43, vcc
	v_rsq_f32_e32 v42, v42
	s_nop 0
	v_mul_f32_e32 v43, 0x45800000, v42
	v_cndmask_b32_e32 v42, v42, v43, vcc
	s_waitcnt vmcnt(4)
	v_mul_f32_e32 v68, v68, v42
	v_mul_f32_e32 v69, v69, v42
	v_mul_f32_e32 v70, v70, v42
	v_mul_f32_e32 v71, v71, v42
	s_waitcnt vmcnt(3)
	v_mul_f32_e32 v72, v72, v42
	v_mul_f32_e32 v73, v73, v42
	v_mul_f32_e32 v74, v74, v42
	v_mul_f32_e32 v75, v75, v42
	s_waitcnt vmcnt(2)
	v_mul_f32_e32 v76, v76, v42
	v_mul_f32_e32 v77, v77, v42
	v_mul_f32_e32 v78, v78, v42
	v_mul_f32_e32 v79, v79, v42
	s_waitcnt vmcnt(1)
	v_mul_f32_e32 v82, v82, v42
	v_mul_f32_e32 v80, v80, v42
	v_mul_f32_e32 v81, v81, v42
	v_mul_f32_e32 v83, v83, v42
	v_mul_f32_e32 v17, v68, v17
	v_mul_f32_e32 v68, v69, v52
	v_mul_f32_e32 v69, v70, v53
	v_mul_f32_e32 v70, v71, v54
	v_mul_f32_e32 v71, v72, v55
	v_mul_f32_e32 v72, v73, v56
	v_mul_f32_e32 v73, v74, v57
	v_mul_f32_e32 v74, v75, v58
	v_mul_f32_e32 v75, v76, v61
	v_mul_f32_e32 v76, v77, v60
	v_mul_f32_e32 v77, v78, v63
	v_mul_f32_e32 v78, v79, v62
	v_mul_f32_e32 v67, v82, v67
	v_cvt_pk_bf16_f32 v60, v17, v68
	v_cvt_pk_bf16_f32 v61, v69, v70
	v_cvt_pk_bf16_f32 v62, v71, v72
	v_cvt_pk_bf16_f32 v63, v73, v74
	v_mul_f32_e32 v79, v80, v65
	v_mul_f32_e32 v80, v81, v64
	v_mul_f32_e32 v81, v83, v66
	v_cvt_pk_bf16_f32 v64, v75, v76
	v_cvt_pk_bf16_f32 v65, v77, v78
	v_cvt_pk_bf16_f32 v66, v79, v80
	v_cvt_pk_bf16_f32 v67, v67, v81
	global_store_dwordx4 v[44:45], v[60:63], off
	global_store_dwordx4 v[44:45], v[64:67], off offset:16
